# static s_setprio 1 for waves 0-3 during GEMM phases only (per-block flips removed)
# speedup vs baseline: 1.0061x; 1.0061x over previous
; #define GRID_BAR() do { if (N_LAUNCHES == 1) xcd_barrier(bar); } while (0)
; __global__ void __launch_bounds__(NWAVES * 64, 2) mega_fwd(Args args) {
;     ...
;     if (IN(PH_GIN)) {
;         pg8::Gemm g{HN, (const bf16*)(KWS + WS_WGI), T, GINM, D}; pg8::StaticOrder S; S.init(T, GINM, F.G, (int)blockIdx.x);
;         pg8::EpiGlaIn E{(bf16*)(KWS + WS_QP), (bf16*)(KWS + WS_KP), (bf16*)(KWS + WS_VB), (bf16*)(KWS + WS_GB), (const float*)(KWS + WS_BC), (const float*)(KWS + WS_RSTD)};
;         for (int rep = 0; rep < NREP(PH_GIN); ++rep) { pg8::gemm_phase<pg8::EpiGlaIn, pg8::StaticOrder, true>(F.lds + RING_OFF, g, S, E); if (rep + 1 < NREP(PH_GIN)) GRID_BAR(); }
.LBB0_237:
	s_cmp_ge_u32 s33, 4
	s_cbranch_scc1 .Lprio_skip_1
	s_setprio 1

; #define LAS __attribute__((address_space(3)))
; template <int LAYER>
; __device__ __forceinline__ void moe_block(Frame& F, const int lo, const int hi, const XcdBarrier& bar) {
;     ...
;     if (IN(pb + 2)) {
;         if (split) {
;             if (N_LAUNCHES != 1) moe_meta(F, LAYER);
;             const int nrt = F.MISC[MI_NRT];
;             { pg8::Gemm g{(const bf16*)H1, (const bf16*)(KWS + WS_WGU) + (size_t)LAYER * NE * 1024 * 2048, nrt * 256, 1024, D};
;               pg8::MoeOrder<true> S{nrt, 4, nrt * 4, F.G, (int)blockIdx.x, (size_t)1024 * 2048 * 2, (const volatile LAS int*)F.MISC, (const int*)(KWS + WS_LIST), 1, 2, 3};
;               pg8::EpiGateUp E{(bf16*)(KWS + WS_ACT), (const float*)(KWS + WS_LRS)};
;               pg8::gemm_phase<pg8::EpiGateUp, pg8::MoeOrder<true>, true>(F.lds + RING_OFF, g, S, E); }
;             { pg8::Gemm g{(const bf16*)(KWS + WS_ACT), (const bf16*)(KWS + WS_WDN) + (size_t)LAYER * NE * 2048 * 512, nrt * 256, 2048, FF};
;               pg8::MoeOrder<false> S{nrt, 8, nrt * 8, F.G, (int)blockIdx.x, (size_t)2048 * 512 * 2, (const volatile LAS int*)F.MISC, (const int*)(KWS + WS_LIST), 2, 0, 0};
;               pg8::EpiDown E{(bf16*)(KWS + WS_Y)};
;               pg8::gemm_phase<pg8::EpiDown, pg8::MoeOrder<false>, true>(F.lds + RING_OFF, g, S, E); }
.LBB0_781:
	s_setprio 0
	s_cmp_ge_u32 s33, 4
	s_cbranch_scc1 .Lprio_skip_4
	s_setprio 1
